# fp8 GEMM epilogues (gate/up, down): bias loads and their address math issued before the epilogue-alignment barrier and the MFMA->VALU pad
# speedup vs baseline: 1.0107x; 1.0028x over previous
.LBB0_49:
	s_add_u32 s36, s26, 0xfffe0080
	s_addc_u32 s37, s27, -1
	s_add_i32 s4, 0, 0x10000
	s_cmp_eq_u32 s92, 4
	s_cselect_b32 s69, s6, s37
	s_cselect_b32 s68, s51, s36
	s_cselect_b32 s37, s49, s74
	s_cselect_b32 s36, s53, s65
	s_add_i32 s93, 0, 0x14000
	v_add_u32_e32 v2, s4, v184
	v_add_u32_e32 v14, s93, v184
	ds_read_b128 v[18:21], v2
	ds_read_b128 v[22:25], v2 offset:1024
	ds_read_b128 v[26:29], v2 offset:2048
	ds_read_b128 v[30:33], v2 offset:3072
	ds_read_b128 v[2:5], v14
	ds_read_b128 v[6:9], v14 offset:1024
	ds_read_b128 v[10:13], v14 offset:2048
	ds_read_b128 v[14:17], v14 offset:3072
	v_lshl_add_u64 v[188:189], s[26:27], 0, v[170:171]
	s_add_i32 m0, s63, 0xc000
	ds_read_b128 v[174:177], v187
	ds_read_b128 v[178:181], v187 offset:1024
	ds_read_b128 v[196:199], v187 offset:2048
	ds_read_b128 v[200:203], v187 offset:3072
	ds_read_b128 v[204:207], v187 offset:4096
	ds_read_b128 v[208:211], v187 offset:5120
	ds_read_b128 v[212:215], v187 offset:6144
	ds_read_b128 v[216:219], v187 offset:7168
	global_load_lds_dwordx4 v[188:189], off
	v_lshl_add_u64 v[188:189], s[26:27], 0, v[172:173]
	s_add_i32 m0, s63, 0xe000
	s_nop 0
	global_load_lds_dwordx4 v[188:189], off
	s_waitcnt vmcnt(8)
	s_waitcnt lgkmcnt(0)
	s_barrier
	s_setprio 1
	s_waitcnt lgkmcnt(0)
	v_mfma_scale_f32_16x16x128_f8f6f4 v[158:161], v[18:25], v[174:181], v[158:161], v191, v191 op_sel_hi:[0,0,0]
	v_mfma_scale_f32_16x16x128_f8f6f4 v[154:157], v[26:33], v[174:181], v[154:157], v191, v191 op_sel_hi:[0,0,0]
	v_mfma_scale_f32_16x16x128_f8f6f4 v[150:153], v[18:25], v[196:203], v[150:153], v191, v191 op_sel_hi:[0,0,0]
	v_mfma_scale_f32_16x16x128_f8f6f4 v[146:149], v[26:33], v[196:203], v[146:149], v191, v191 op_sel_hi:[0,0,0]
	v_mfma_scale_f32_16x16x128_f8f6f4 v[126:129], v[18:25], v[204:211], v[126:129], v191, v191 op_sel_hi:[0,0,0]
	v_mfma_scale_f32_16x16x128_f8f6f4 v[122:125], v[26:33], v[204:211], v[122:125], v191, v191 op_sel_hi:[0,0,0]
	v_mfma_scale_f32_16x16x128_f8f6f4 v[118:121], v[18:25], v[212:219], v[118:121], v191, v191 op_sel_hi:[0,0,0]
	v_mfma_scale_f32_16x16x128_f8f6f4 v[114:117], v[26:33], v[212:219], v[114:117], v191, v191 op_sel_hi:[0,0,0]
	s_setprio 0
	s_setprio 1
	v_mfma_scale_f32_16x16x128_f8f6f4 v[142:145], v[2:9], v[174:181], v[142:145], v191, v191 op_sel_hi:[0,0,0]
	v_mfma_scale_f32_16x16x128_f8f6f4 v[138:141], v[10:17], v[174:181], v[138:141], v191, v191 op_sel_hi:[0,0,0]
	v_mfma_scale_f32_16x16x128_f8f6f4 v[134:137], v[2:9], v[196:203], v[134:137], v191, v191 op_sel_hi:[0,0,0]
	v_mfma_scale_f32_16x16x128_f8f6f4 v[130:133], v[10:17], v[196:203], v[130:133], v191, v191 op_sel_hi:[0,0,0]
	v_mfma_scale_f32_16x16x128_f8f6f4 v[110:113], v[2:9], v[204:211], v[110:113], v191, v191 op_sel_hi:[0,0,0]
	v_mfma_scale_f32_16x16x128_f8f6f4 v[106:109], v[10:17], v[204:211], v[106:109], v191, v191 op_sel_hi:[0,0,0]
	v_mfma_scale_f32_16x16x128_f8f6f4 v[102:105], v[2:9], v[212:219], v[102:105], v191, v191 op_sel_hi:[0,0,0]
	v_mfma_scale_f32_16x16x128_f8f6f4 v[98:101], v[10:17], v[212:219], v[98:101], v191, v191 op_sel_hi:[0,0,0]
	s_setprio 0
	s_barrier
	s_add_i32 s4, s4, s45
	v_lshl_add_u64 v[174:175], s[36:37], 0, v[0:1]
	s_mov_b32 m0, s4
	ds_read_b128 v[196:199], v187 offset:16384
	ds_read_b128 v[200:203], v187 offset:17408
	ds_read_b128 v[204:207], v187 offset:18432
	ds_read_b128 v[208:211], v187 offset:19456
	ds_read_b128 v[212:215], v187 offset:20480
	ds_read_b128 v[216:219], v187 offset:21504
	ds_read_b128 v[234:237], v187 offset:22528
	ds_read_b128 v[238:241], v187 offset:23552
	global_load_lds_dwordx4 v[174:175], off
	s_add_i32 m0, s4, 0x2000
	s_add_u32 s86, s36, 0x20000
	v_lshl_add_u64 v[176:177], s[36:37], 0, v[166:167]
	s_addc_u32 s87, s37, 0
	s_add_i32 s4, s93, s45
	global_load_lds_dwordx4 v[176:177], off
	v_lshl_add_u64 v[178:179], s[86:87], 0, v[0:1]
	s_mov_b32 m0, s4
	v_lshl_add_u64 v[180:181], s[68:69], 0, v[164:165]
	global_load_lds_dwordx4 v[178:179], off
	v_lshl_add_u64 v[178:179], s[86:87], 0, v[166:167]
	s_add_i32 m0, s4, 0x2000
	s_nop 0
	global_load_lds_dwordx4 v[178:179], off
	v_lshl_add_u64 v[178:179], s[68:69], 0, v[162:163]
	s_mov_b32 m0, s63
	s_nop 0
	global_load_lds_dwordx4 v[178:179], off
	s_mov_b32 m0, s67
	s_nop 0
	global_load_lds_dwordx4 v[180:181], off
	s_waitcnt vmcnt(8)
	s_waitcnt lgkmcnt(0)
	s_barrier
	s_setprio 1
	s_waitcnt lgkmcnt(0)
	v_mfma_scale_f32_16x16x128_f8f6f4 v[94:97], v[18:25], v[196:203], v[94:97], v191, v191 op_sel_hi:[0,0,0]
	v_mfma_scale_f32_16x16x128_f8f6f4 v[90:93], v[26:33], v[196:203], v[90:93], v191, v191 op_sel_hi:[0,0,0]
	v_mfma_scale_f32_16x16x128_f8f6f4 v[86:89], v[18:25], v[204:211], v[86:89], v191, v191 op_sel_hi:[0,0,0]
	v_mfma_scale_f32_16x16x128_f8f6f4 v[82:85], v[26:33], v[204:211], v[82:85], v191, v191 op_sel_hi:[0,0,0]
	v_mfma_scale_f32_16x16x128_f8f6f4 v[62:65], v[18:25], v[212:219], v[62:65], v191, v191 op_sel_hi:[0,0,0]
	v_mfma_scale_f32_16x16x128_f8f6f4 v[58:61], v[26:33], v[212:219], v[58:61], v191, v191 op_sel_hi:[0,0,0]
	v_mfma_scale_f32_16x16x128_f8f6f4 v[54:57], v[18:25], v[234:241], v[54:57], v191, v191 op_sel_hi:[0,0,0]
	v_mfma_scale_f32_16x16x128_f8f6f4 v[50:53], v[26:33], v[234:241], v[50:53], v191, v191 op_sel_hi:[0,0,0]
	s_setprio 0
	s_setprio 1
	v_mfma_scale_f32_16x16x128_f8f6f4 v[78:81], v[2:9], v[196:203], v[78:81], v191, v191 op_sel_hi:[0,0,0]
	v_mfma_scale_f32_16x16x128_f8f6f4 v[74:77], v[10:17], v[196:203], v[74:77], v191, v191 op_sel_hi:[0,0,0]
	v_mfma_scale_f32_16x16x128_f8f6f4 v[70:73], v[2:9], v[204:211], v[70:73], v191, v191 op_sel_hi:[0,0,0]
	v_mfma_scale_f32_16x16x128_f8f6f4 v[66:69], v[10:17], v[204:211], v[66:69], v191, v191 op_sel_hi:[0,0,0]
	v_mfma_scale_f32_16x16x128_f8f6f4 v[46:49], v[2:9], v[212:219], v[46:49], v191, v191 op_sel_hi:[0,0,0]
	v_mfma_scale_f32_16x16x128_f8f6f4 v[42:45], v[10:17], v[212:219], v[42:45], v191, v191 op_sel_hi:[0,0,0]
	v_mfma_scale_f32_16x16x128_f8f6f4 v[38:41], v[2:9], v[234:241], v[38:41], v191, v191 op_sel_hi:[0,0,0]
	v_mfma_scale_f32_16x16x128_f8f6f4 v[34:37], v[10:17], v[234:241], v[34:37], v191, v191 op_sel_hi:[0,0,0]
	s_setprio 0
	s_barrier
	s_add_i32 s4, 0, 0x18000
	s_add_i32 s86, 0, 0x1c000
	v_add_u32_e32 v14, s4, v184
	v_add_u32_e32 v30, s86, v184
	ds_read_b128 v[2:5], v14
	ds_read_b128 v[6:9], v14 offset:1024
	ds_read_b128 v[10:13], v14 offset:2048
	ds_read_b128 v[14:17], v14 offset:3072
	ds_read_b128 v[18:21], v30
	ds_read_b128 v[22:25], v30 offset:1024
	ds_read_b128 v[26:29], v30 offset:2048
	ds_read_b128 v[30:33], v30 offset:3072
	s_add_u32 s68, s68, 0x20000
	s_addc_u32 s69, s69, 0
	s_mov_b32 m0, s73
	v_lshl_add_u64 v[188:189], s[68:69], 0, v[162:163]
	ds_read_b128 v[196:199], v187 offset:32768
	ds_read_b128 v[200:203], v187 offset:33792
	ds_read_b128 v[204:207], v187 offset:34816
	ds_read_b128 v[208:211], v187 offset:35840
	ds_read_b128 v[212:215], v187 offset:36864
	ds_read_b128 v[216:219], v187 offset:37888
	ds_read_b128 v[234:237], v187 offset:38912
	ds_read_b128 v[238:241], v187 offset:39936
	global_load_lds_dwordx4 v[188:189], off
	v_lshl_add_u64 v[188:189], s[68:69], 0, v[164:165]
	s_mov_b32 m0, s75
	s_nop 0
	global_load_lds_dwordx4 v[188:189], off
	s_waitcnt vmcnt(8)
	s_waitcnt lgkmcnt(0)
	s_barrier
	s_setprio 1
	s_waitcnt lgkmcnt(0)
	v_mfma_scale_f32_16x16x128_f8f6f4 v[158:161], v[2:9], v[196:203], v[158:161], v191, v191 op_sel_hi:[0,0,0]
	v_mfma_scale_f32_16x16x128_f8f6f4 v[154:157], v[10:17], v[196:203], v[154:157], v191, v191 op_sel_hi:[0,0,0]
	v_mfma_scale_f32_16x16x128_f8f6f4 v[150:153], v[2:9], v[204:211], v[150:153], v191, v191 op_sel_hi:[0,0,0]
	v_mfma_scale_f32_16x16x128_f8f6f4 v[146:149], v[10:17], v[204:211], v[146:149], v191, v191 op_sel_hi:[0,0,0]
	v_mfma_scale_f32_16x16x128_f8f6f4 v[126:129], v[2:9], v[212:219], v[126:129], v191, v191 op_sel_hi:[0,0,0]
	v_mfma_scale_f32_16x16x128_f8f6f4 v[122:125], v[10:17], v[212:219], v[122:125], v191, v191 op_sel_hi:[0,0,0]
	v_mfma_scale_f32_16x16x128_f8f6f4 v[118:121], v[2:9], v[234:241], v[118:121], v191, v191 op_sel_hi:[0,0,0]
	v_mfma_scale_f32_16x16x128_f8f6f4 v[114:117], v[10:17], v[234:241], v[114:117], v191, v191 op_sel_hi:[0,0,0]
	s_setprio 0
	s_setprio 1
	v_mfma_scale_f32_16x16x128_f8f6f4 v[142:145], v[18:25], v[196:203], v[142:145], v191, v191 op_sel_hi:[0,0,0]
	v_mfma_scale_f32_16x16x128_f8f6f4 v[138:141], v[26:33], v[196:203], v[138:141], v191, v191 op_sel_hi:[0,0,0]
	v_mfma_scale_f32_16x16x128_f8f6f4 v[134:137], v[18:25], v[204:211], v[134:137], v191, v191 op_sel_hi:[0,0,0]
	v_mfma_scale_f32_16x16x128_f8f6f4 v[130:133], v[26:33], v[204:211], v[130:133], v191, v191 op_sel_hi:[0,0,0]
	v_mfma_scale_f32_16x16x128_f8f6f4 v[110:113], v[18:25], v[212:219], v[110:113], v191, v191 op_sel_hi:[0,0,0]
	v_mfma_scale_f32_16x16x128_f8f6f4 v[106:109], v[26:33], v[212:219], v[106:109], v191, v191 op_sel_hi:[0,0,0]
	v_mfma_scale_f32_16x16x128_f8f6f4 v[102:105], v[18:25], v[234:241], v[102:105], v191, v191 op_sel_hi:[0,0,0]
	v_mfma_scale_f32_16x16x128_f8f6f4 v[98:101], v[26:33], v[234:241], v[98:101], v191, v191 op_sel_hi:[0,0,0]
	s_setprio 0
	s_barrier
	s_add_i32 s4, s4, s45
	v_lshl_add_u64 v[174:175], v[174:175], 0, s[22:23]
	s_mov_b32 m0, s4
	ds_read_b128 v[196:199], v187 offset:49152
	ds_read_b128 v[200:203], v187 offset:50176
	ds_read_b128 v[204:207], v187 offset:51200
	ds_read_b128 v[208:211], v187 offset:52224
	ds_read_b128 v[212:215], v187 offset:53248
	ds_read_b128 v[216:219], v187 offset:54272
	ds_read_b128 v[234:237], v187 offset:55296
	ds_read_b128 v[238:241], v187 offset:56320
	global_load_lds_dwordx4 v[174:175], off
	s_add_i32 m0, s4, 0x2000
	s_add_u32 s36, s36, 0x20080
	v_lshl_add_u64 v[174:175], v[176:177], 0, s[22:23]
	s_addc_u32 s37, s37, 0
	s_add_i32 s4, s86, s45
	global_load_lds_dwordx4 v[174:175], off
	v_lshl_add_u64 v[174:175], s[36:37], 0, v[0:1]
	s_mov_b32 m0, s4
	s_nop 0
	global_load_lds_dwordx4 v[174:175], off
	v_lshl_add_u64 v[174:175], s[36:37], 0, v[166:167]
	s_add_i32 m0, s4, 0x2000
	s_nop 0
	global_load_lds_dwordx4 v[174:175], off
	v_lshl_add_u64 v[174:175], v[178:179], 0, s[22:23]
	s_mov_b32 m0, s79
	s_nop 0
	global_load_lds_dwordx4 v[174:175], off
	v_lshl_add_u64 v[174:175], v[180:181], 0, s[22:23]
	s_mov_b32 m0, s82
	s_nop 0
	global_load_lds_dwordx4 v[174:175], off
	s_waitcnt vmcnt(8)
	s_waitcnt lgkmcnt(0)
	s_barrier
	s_setprio 1
	s_waitcnt lgkmcnt(0)
	v_mfma_scale_f32_16x16x128_f8f6f4 v[94:97], v[2:9], v[196:203], v[94:97], v191, v191 op_sel_hi:[0,0,0]
	v_mfma_scale_f32_16x16x128_f8f6f4 v[90:93], v[10:17], v[196:203], v[90:93], v191, v191 op_sel_hi:[0,0,0]
	v_mfma_scale_f32_16x16x128_f8f6f4 v[86:89], v[2:9], v[204:211], v[86:89], v191, v191 op_sel_hi:[0,0,0]
	v_mfma_scale_f32_16x16x128_f8f6f4 v[82:85], v[10:17], v[204:211], v[82:85], v191, v191 op_sel_hi:[0,0,0]
	v_mfma_scale_f32_16x16x128_f8f6f4 v[62:65], v[2:9], v[212:219], v[62:65], v191, v191 op_sel_hi:[0,0,0]
	v_mfma_scale_f32_16x16x128_f8f6f4 v[58:61], v[10:17], v[212:219], v[58:61], v191, v191 op_sel_hi:[0,0,0]
	v_mfma_scale_f32_16x16x128_f8f6f4 v[54:57], v[2:9], v[234:241], v[54:57], v191, v191 op_sel_hi:[0,0,0]
	v_mfma_scale_f32_16x16x128_f8f6f4 v[50:53], v[10:17], v[234:241], v[50:53], v191, v191 op_sel_hi:[0,0,0]
	s_setprio 0
	s_setprio 1
	v_mfma_scale_f32_16x16x128_f8f6f4 v[78:81], v[18:25], v[196:203], v[78:81], v191, v191 op_sel_hi:[0,0,0]
	v_mfma_scale_f32_16x16x128_f8f6f4 v[74:77], v[26:33], v[196:203], v[74:77], v191, v191 op_sel_hi:[0,0,0]
	v_mfma_scale_f32_16x16x128_f8f6f4 v[70:73], v[18:25], v[204:211], v[70:73], v191, v191 op_sel_hi:[0,0,0]
	v_mfma_scale_f32_16x16x128_f8f6f4 v[66:69], v[26:33], v[204:211], v[66:69], v191, v191 op_sel_hi:[0,0,0]
	v_mfma_scale_f32_16x16x128_f8f6f4 v[46:49], v[18:25], v[212:219], v[46:49], v191, v191 op_sel_hi:[0,0,0]
	v_mfma_scale_f32_16x16x128_f8f6f4 v[42:45], v[26:33], v[212:219], v[42:45], v191, v191 op_sel_hi:[0,0,0]
	v_mfma_scale_f32_16x16x128_f8f6f4 v[38:41], v[18:25], v[234:241], v[38:41], v191, v191 op_sel_hi:[0,0,0]
	v_mfma_scale_f32_16x16x128_f8f6f4 v[34:37], v[26:33], v[234:241], v[34:37], v191, v191 op_sel_hi:[0,0,0]
	s_setprio 0
	s_barrier
	s_add_i32 s92, s92, 2
	s_add_u32 s26, s26, 0x100
	s_addc_u32 s27, s27, 0
	s_add_u32 s65, s65, 0x100
	s_addc_u32 s74, s74, 0
	s_cmp_gt_u32 s92, 5
	s_cbranch_scc0 .LBB0_49
	s_ashr_i32 s65, s64, 31
	s_lshl_b32 s26, s66, 8
	s_lshl_b64 s[36:37], s[64:65], 12
	v_or_b32_e32 v2, s26, v185
	s_add_u32 s36, s5, s36
	s_addc_u32 s37, s78, s37
	v_ashrrev_i32_e32 v3, 31, v2
	v_lshl_add_u64 v[6:7], v[2:3], 2, s[36:37]
	global_load_dwordx4 v[10:13], v[6:7], off offset:16
	global_load_dwordx4 v[14:17], v[6:7], off
	global_load_dwordx4 v[2:5], v[6:7], off offset:528
	s_nop 0
	global_load_dwordx4 v[6:9], v[6:7], off offset:512
	s_and_b64 vcc, exec, s[42:43]
	s_cbranch_vccz .LBB0_52
	s_barrier
.LBB0_52:
	s_nop 15
	s_nop 15
	v_mov_b32_e32 v18, v1
	v_mov_b32_e32 v19, v1
	v_lshl_add_u32 v22, s62, 8, v186
	v_ashrrev_i32_e32 v23, 31, v22
	s_ashr_i32 s27, s26, 31
	s_andn2_b64 vcc, exec, s[54:55]
	s_waitcnt vmcnt(0)
	v_pk_fma_f32 v[28:29], v[154:155], s[24:25], v[10:11] op_sel_hi:[1,0,1]
	v_pk_fma_f32 v[24:25], v[158:159], s[24:25], v[14:15] op_sel_hi:[1,0,1]
	v_cvt_pk_fp8_f32 v19, v28, v29
	v_cvt_pk_fp8_f32 v18, v24, v25
	v_pk_fma_f32 v[20:21], v[160:161], s[24:25], v[16:17] op_sel_hi:[1,0,1]
	v_pk_fma_f32 v[26:27], v[156:157], s[24:25], v[12:13] op_sel_hi:[1,0,1]
	v_pk_fma_f32 v[30:31], v[146:147], s[24:25], v[10:11] op_sel_hi:[1,0,1]
	v_cvt_pk_fp8_f32 v18, v20, v21 op_sel:[0,0,1]
	v_cvt_pk_fp8_f32 v19, v26, v27 op_sel:[0,0,1]
	v_pk_fma_f32 v[26:27], v[150:151], s[24:25], v[14:15] op_sel_hi:[1,0,1]
	v_mov_b32_e32 v20, v1
	v_mov_b32_e32 v21, v1
	v_cvt_pk_fp8_f32 v20, v26, v27
	v_cvt_pk_fp8_f32 v21, v30, v31
	v_pk_fma_f32 v[24:25], v[152:153], s[24:25], v[16:17] op_sel_hi:[1,0,1]
	v_pk_fma_f32 v[28:29], v[148:149], s[24:25], v[12:13] op_sel_hi:[1,0,1]
	v_cvt_pk_fp8_f32 v20, v24, v25 op_sel:[0,0,1]
	v_cvt_pk_fp8_f32 v21, v28, v29 op_sel:[0,0,1]
	v_lshlrev_b64 v[24:25], 10, v[22:23]
	v_lshl_add_u64 v[24:25], s[40:41], 0, v[24:25]
	v_lshl_add_u64 v[24:25], v[24:25], 0, s[26:27]
	v_lshl_add_u64 v[24:25], v[24:25], 0, s[94:95]
	v_permlane16_swap_b32_e32 v18, v20
	v_permlane16_swap_b32_e32 v19, v21
	v_lshl_add_u64 v[24:25], v[24:25], 0, v[168:169]
	global_store_dwordx4 v[24:25], v[18:21], off
	v_pk_fma_f32 v[26:27], v[142:143], s[24:25], v[6:7] op_sel_hi:[1,0,1]
	v_pk_fma_f32 v[30:31], v[138:139], s[24:25], v[2:3] op_sel_hi:[1,0,1]
	v_mov_b32_e32 v18, v1
	v_mov_b32_e32 v19, v1
	v_cvt_pk_fp8_f32 v18, v26, v27
	v_cvt_pk_fp8_f32 v19, v30, v31
	v_pk_fma_f32 v[20:21], v[144:145], s[24:25], v[8:9] op_sel_hi:[1,0,1]
	v_pk_fma_f32 v[28:29], v[140:141], s[24:25], v[4:5] op_sel_hi:[1,0,1]
	v_cvt_pk_fp8_f32 v18, v20, v21 op_sel:[0,0,1]
	v_cvt_pk_fp8_f32 v19, v28, v29 op_sel:[0,0,1]
	v_pk_fma_f32 v[28:29], v[134:135], s[24:25], v[6:7] op_sel_hi:[1,0,1]
	v_pk_fma_f32 v[32:33], v[130:131], s[24:25], v[2:3] op_sel_hi:[1,0,1]
	v_mov_b32_e32 v20, v1
	v_mov_b32_e32 v21, v1
	v_cvt_pk_fp8_f32 v20, v28, v29
	v_cvt_pk_fp8_f32 v21, v32, v33
	v_pk_fma_f32 v[26:27], v[136:137], s[24:25], v[8:9] op_sel_hi:[1,0,1]
	v_pk_fma_f32 v[30:31], v[132:133], s[24:25], v[4:5] op_sel_hi:[1,0,1]
	v_cvt_pk_fp8_f32 v20, v26, v27 op_sel:[0,0,1]
	v_cvt_pk_fp8_f32 v21, v30, v31 op_sel:[0,0,1]
	v_pk_fma_f32 v[26:27], v[126:127], s[24:25], v[14:15] op_sel_hi:[1,0,1]
	v_pk_fma_f32 v[30:31], v[122:123], s[24:25], v[10:11] op_sel_hi:[1,0,1]
	v_permlane16_swap_b32_e32 v18, v20
	v_permlane16_swap_b32_e32 v19, v21
	global_store_dwordx4 v[24:25], v[18:21], off offset:128
	v_pk_fma_f32 v[32:33], v[114:115], s[24:25], v[10:11] op_sel_hi:[1,0,1]
	v_or_b32_e32 v24, 32, v22
	v_mov_b32_e32 v18, v1
	v_cvt_pk_fp8_f32 v18, v26, v27
	v_pk_fma_f32 v[20:21], v[128:129], s[24:25], v[16:17] op_sel_hi:[1,0,1]
	v_mov_b32_e32 v19, v1
	v_cvt_pk_fp8_f32 v19, v30, v31
	v_cvt_pk_fp8_f32 v18, v20, v21 op_sel:[0,0,1]
	v_pk_fma_f32 v[30:31], v[118:119], s[24:25], v[14:15] op_sel_hi:[1,0,1]
	v_mov_b32_e32 v20, v1
	v_mov_b32_e32 v21, v1
	v_cvt_pk_fp8_f32 v20, v30, v31
	v_cvt_pk_fp8_f32 v21, v32, v33
	v_pk_fma_f32 v[28:29], v[124:125], s[24:25], v[12:13] op_sel_hi:[1,0,1]
	v_ashrrev_i32_e32 v25, 31, v24
	v_cvt_pk_fp8_f32 v19, v28, v29 op_sel:[0,0,1]
	v_pk_fma_f32 v[28:29], v[120:121], s[24:25], v[16:17] op_sel_hi:[1,0,1]
	v_pk_fma_f32 v[26:27], v[116:117], s[24:25], v[12:13] op_sel_hi:[1,0,1]
	v_cvt_pk_fp8_f32 v20, v28, v29 op_sel:[0,0,1]
	v_cvt_pk_fp8_f32 v21, v26, v27 op_sel:[0,0,1]
	v_lshlrev_b64 v[24:25], 10, v[24:25]
	v_lshl_add_u64 v[24:25], s[40:41], 0, v[24:25]
	v_lshl_add_u64 v[24:25], v[24:25], 0, s[26:27]
	v_lshl_add_u64 v[24:25], v[24:25], 0, s[94:95]
	v_permlane16_swap_b32_e32 v18, v20
	v_permlane16_swap_b32_e32 v19, v21
	v_lshl_add_u64 v[24:25], v[24:25], 0, v[168:169]
	global_store_dwordx4 v[24:25], v[18:21], off
	v_pk_fma_f32 v[26:27], v[110:111], s[24:25], v[6:7] op_sel_hi:[1,0,1]
	v_pk_fma_f32 v[30:31], v[106:107], s[24:25], v[2:3] op_sel_hi:[1,0,1]
	v_mov_b32_e32 v18, v1
	v_mov_b32_e32 v19, v1
	v_cvt_pk_fp8_f32 v18, v26, v27
	v_cvt_pk_fp8_f32 v19, v30, v31
	v_pk_fma_f32 v[20:21], v[112:113], s[24:25], v[8:9] op_sel_hi:[1,0,1]
	v_pk_fma_f32 v[28:29], v[108:109], s[24:25], v[4:5] op_sel_hi:[1,0,1]
	v_cvt_pk_fp8_f32 v18, v20, v21 op_sel:[0,0,1]
	v_cvt_pk_fp8_f32 v19, v28, v29 op_sel:[0,0,1]
	v_pk_fma_f32 v[28:29], v[102:103], s[24:25], v[6:7] op_sel_hi:[1,0,1]
	v_pk_fma_f32 v[32:33], v[98:99], s[24:25], v[2:3] op_sel_hi:[1,0,1]
	v_mov_b32_e32 v20, v1
	v_mov_b32_e32 v21, v1
	v_cvt_pk_fp8_f32 v20, v28, v29
	v_cvt_pk_fp8_f32 v21, v32, v33
	v_pk_fma_f32 v[26:27], v[104:105], s[24:25], v[8:9] op_sel_hi:[1,0,1]
	v_pk_fma_f32 v[30:31], v[100:101], s[24:25], v[4:5] op_sel_hi:[1,0,1]
	v_cvt_pk_fp8_f32 v20, v26, v27 op_sel:[0,0,1]
	v_cvt_pk_fp8_f32 v21, v30, v31 op_sel:[0,0,1]
	v_pk_fma_f32 v[26:27], v[94:95], s[24:25], v[14:15] op_sel_hi:[1,0,1]
	v_pk_fma_f32 v[30:31], v[90:91], s[24:25], v[10:11] op_sel_hi:[1,0,1]
	v_permlane16_swap_b32_e32 v18, v20
	v_permlane16_swap_b32_e32 v19, v21
	global_store_dwordx4 v[24:25], v[18:21], off offset:128
	v_pk_fma_f32 v[28:29], v[92:93], s[24:25], v[12:13] op_sel_hi:[1,0,1]
	v_pk_fma_f32 v[32:33], v[82:83], s[24:25], v[10:11] op_sel_hi:[1,0,1]
	v_mov_b32_e32 v18, v1
	v_mov_b32_e32 v19, v1
	v_cvt_pk_fp8_f32 v18, v26, v27
	v_cvt_pk_fp8_f32 v19, v30, v31
	v_pk_fma_f32 v[20:21], v[96:97], s[24:25], v[16:17] op_sel_hi:[1,0,1]
	v_add_u32_e32 v24, 0x80, v22
	v_cvt_pk_fp8_f32 v18, v20, v21 op_sel:[0,0,1]
	v_cvt_pk_fp8_f32 v19, v28, v29 op_sel:[0,0,1]
	v_pk_fma_f32 v[28:29], v[86:87], s[24:25], v[14:15] op_sel_hi:[1,0,1]
	v_mov_b32_e32 v20, v1
	v_mov_b32_e32 v21, v1
	v_cvt_pk_fp8_f32 v20, v28, v29
	v_cvt_pk_fp8_f32 v21, v32, v33
	v_ashrrev_i32_e32 v25, 31, v24
	v_pk_fma_f32 v[26:27], v[88:89], s[24:25], v[16:17] op_sel_hi:[1,0,1]
	v_pk_fma_f32 v[30:31], v[84:85], s[24:25], v[12:13] op_sel_hi:[1,0,1]
	v_cvt_pk_fp8_f32 v20, v26, v27 op_sel:[0,0,1]
	v_cvt_pk_fp8_f32 v21, v30, v31 op_sel:[0,0,1]
	v_lshlrev_b64 v[24:25], 10, v[24:25]
	v_lshl_add_u64 v[24:25], s[40:41], 0, v[24:25]
	v_lshl_add_u64 v[24:25], v[24:25], 0, s[26:27]
	v_lshl_add_u64 v[24:25], v[24:25], 0, s[94:95]
	v_permlane16_swap_b32_e32 v18, v20
	v_permlane16_swap_b32_e32 v19, v21
	v_lshl_add_u64 v[24:25], v[24:25], 0, v[168:169]
	global_store_dwordx4 v[24:25], v[18:21], off
	v_pk_fma_f32 v[26:27], v[78:79], s[24:25], v[6:7] op_sel_hi:[1,0,1]
	v_pk_fma_f32 v[30:31], v[74:75], s[24:25], v[2:3] op_sel_hi:[1,0,1]
	v_mov_b32_e32 v18, v1
	v_mov_b32_e32 v19, v1
	v_cvt_pk_fp8_f32 v18, v26, v27
	v_cvt_pk_fp8_f32 v19, v30, v31
	v_pk_fma_f32 v[20:21], v[80:81], s[24:25], v[8:9] op_sel_hi:[1,0,1]
	v_pk_fma_f32 v[28:29], v[76:77], s[24:25], v[4:5] op_sel_hi:[1,0,1]
	v_cvt_pk_fp8_f32 v18, v20, v21 op_sel:[0,0,1]
	v_cvt_pk_fp8_f32 v19, v28, v29 op_sel:[0,0,1]
	v_pk_fma_f32 v[28:29], v[70:71], s[24:25], v[6:7] op_sel_hi:[1,0,1]
	v_pk_fma_f32 v[32:33], v[66:67], s[24:25], v[2:3] op_sel_hi:[1,0,1]
	v_mov_b32_e32 v20, v1
	v_mov_b32_e32 v21, v1
	v_cvt_pk_fp8_f32 v20, v28, v29
	v_cvt_pk_fp8_f32 v21, v32, v33
	v_pk_fma_f32 v[26:27], v[72:73], s[24:25], v[8:9] op_sel_hi:[1,0,1]
	v_pk_fma_f32 v[30:31], v[68:69], s[24:25], v[4:5] op_sel_hi:[1,0,1]
	v_cvt_pk_fp8_f32 v20, v26, v27 op_sel:[0,0,1]
	v_cvt_pk_fp8_f32 v21, v30, v31 op_sel:[0,0,1]
	v_add_u32_e32 v22, 0xa0, v22
	v_ashrrev_i32_e32 v23, 31, v22
	v_permlane16_swap_b32_e32 v18, v20
	v_permlane16_swap_b32_e32 v19, v21
	global_store_dwordx4 v[24:25], v[18:21], off offset:128
	v_pk_fma_f32 v[24:25], v[62:63], s[24:25], v[14:15] op_sel_hi:[1,0,1]
	v_pk_fma_f32 v[28:29], v[58:59], s[24:25], v[10:11] op_sel_hi:[1,0,1]
	v_mov_b32_e32 v18, v1
	v_cvt_pk_fp8_f32 v18, v24, v25
	v_pk_fma_f32 v[20:21], v[64:65], s[24:25], v[16:17] op_sel_hi:[1,0,1]
	v_mov_b32_e32 v19, v1
	v_pk_fma_f32 v[14:15], v[54:55], s[24:25], v[14:15] op_sel_hi:[1,0,1]
	v_cvt_pk_fp8_f32 v18, v20, v21 op_sel:[0,0,1]
	v_pk_fma_f32 v[10:11], v[50:51], s[24:25], v[10:11] op_sel_hi:[1,0,1]
	v_mov_b32_e32 v20, v1
	v_mov_b32_e32 v21, v1
	v_cvt_pk_fp8_f32 v19, v28, v29
	v_cvt_pk_fp8_f32 v20, v14, v15
	v_cvt_pk_fp8_f32 v21, v10, v11
	v_lshlrev_b64 v[10:11], 10, v[22:23]
	v_lshl_add_u64 v[10:11], s[40:41], 0, v[10:11]
	v_lshl_add_u64 v[10:11], v[10:11], 0, s[26:27]
	v_pk_fma_f32 v[26:27], v[60:61], s[24:25], v[12:13] op_sel_hi:[1,0,1]
	v_pk_fma_f32 v[16:17], v[56:57], s[24:25], v[16:17] op_sel_hi:[1,0,1]
	v_pk_fma_f32 v[12:13], v[52:53], s[24:25], v[12:13] op_sel_hi:[1,0,1]
	v_lshl_add_u64 v[10:11], v[10:11], 0, s[94:95]
	v_cvt_pk_fp8_f32 v19, v26, v27 op_sel:[0,0,1]
	v_cvt_pk_fp8_f32 v20, v16, v17 op_sel:[0,0,1]
	v_cvt_pk_fp8_f32 v21, v12, v13 op_sel:[0,0,1]
	v_lshl_add_u64 v[14:15], v[10:11], 0, v[168:169]
	v_pk_fma_f32 v[16:17], v[46:47], s[24:25], v[6:7] op_sel_hi:[1,0,1]
	v_mov_b32_e32 v10, v1
	v_cvt_pk_fp8_f32 v10, v16, v17
	v_permlane16_swap_b32_e32 v18, v20
	v_permlane16_swap_b32_e32 v19, v21
	v_pk_fma_f32 v[12:13], v[48:49], s[24:25], v[8:9] op_sel_hi:[1,0,1]
	global_store_dwordx4 v[14:15], v[18:21], off
	v_cvt_pk_fp8_f32 v10, v12, v13 op_sel:[0,0,1]
	v_mov_b32_e32 v11, v1
	v_pk_fma_f32 v[20:21], v[42:43], s[24:25], v[2:3] op_sel_hi:[1,0,1]
	v_pk_fma_f32 v[6:7], v[38:39], s[24:25], v[6:7] op_sel_hi:[1,0,1]
	v_pk_fma_f32 v[2:3], v[34:35], s[24:25], v[2:3] op_sel_hi:[1,0,1]
	v_mov_b32_e32 v12, v1
	v_mov_b32_e32 v13, v1
	v_cvt_pk_fp8_f32 v11, v20, v21
	v_cvt_pk_fp8_f32 v12, v6, v7
	v_cvt_pk_fp8_f32 v13, v2, v3
	v_pk_fma_f32 v[18:19], v[44:45], s[24:25], v[4:5] op_sel_hi:[1,0,1]
	v_pk_fma_f32 v[8:9], v[40:41], s[24:25], v[8:9] op_sel_hi:[1,0,1]
	v_pk_fma_f32 v[4:5], v[36:37], s[24:25], v[4:5] op_sel_hi:[1,0,1]
	v_cvt_pk_fp8_f32 v11, v18, v19 op_sel:[0,0,1]
	v_cvt_pk_fp8_f32 v12, v8, v9 op_sel:[0,0,1]
	v_cvt_pk_fp8_f32 v13, v4, v5 op_sel:[0,0,1]
	s_mov_b64 s[26:27], -1
	v_permlane16_swap_b32_e32 v10, v12
	v_permlane16_swap_b32_e32 v11, v13
	global_store_dwordx4 v[14:15], v[10:13], off offset:128
	s_cbranch_vccnz .LBB0_39
	s_andn2_b64 vcc, exec, s[38:39]
	s_cbranch_vccnz .LBB0_38
	s_barrier
	s_branch .LBB0_38

.LBB0_249:
	s_add_u32 s4, s46, s26
	s_addc_u32 s36, s47, s27
	s_add_u32 s69, s4, 0x2e000100
	s_addc_u32 s70, s36, 0
	s_add_u32 s74, s61, s26
	s_addc_u32 s86, s63, s27
	s_add_i32 s4, 0, 0x10000
	s_cmpk_eq_i32 s26, 0x300
	s_cselect_b64 vcc, -1, 0
	s_and_b64 s[36:37], vcc, exec
	s_cselect_b32 s71, s41, s70
	s_cselect_b32 s70, s40, s69
	v_add_u32_e32 v0, s4, v200
	s_cselect_b32 s37, s6, s86
	s_cselect_b32 s36, s31, s74
	s_add_i32 s69, 0, 0x14000
	ds_read_b128 v[18:21], v0
	ds_read_b128 v[22:25], v0 offset:1024
	ds_read_b128 v[26:29], v0 offset:2048
	ds_read_b128 v[30:33], v0 offset:3072
	v_add_u32_e32 v0, s69, v200
	ds_read_b128 v[2:5], v0
	ds_read_b128 v[6:9], v0 offset:1024
	ds_read_b128 v[10:13], v0 offset:2048
	ds_read_b128 v[14:17], v0 offset:3072
	v_lshl_add_u64 v[222:223], v[178:179], 0, s[26:27]
	s_add_i32 m0, s93, 0xc000
	ds_read_b128 v[180:183], v201
	ds_read_b128 v[184:187], v201 offset:1024
	ds_read_b128 v[206:209], v201 offset:2048
	ds_read_b128 v[210:213], v201 offset:3072
	ds_read_b128 v[214:217], v201 offset:4096
	ds_read_b128 v[218:221], v201 offset:5120
	ds_read_b128 v[234:237], v201 offset:6144
	ds_read_b128 v[238:241], v201 offset:7168
	global_load_lds_dwordx4 v[222:223], off
	v_lshl_add_u64 v[222:223], v[176:177], 0, s[26:27]
	s_add_i32 m0, s93, 0xe000
	s_nop 0
	global_load_lds_dwordx4 v[222:223], off
	s_waitcnt vmcnt(8)
	s_waitcnt lgkmcnt(0)
	s_barrier
	s_setprio 1
	s_waitcnt lgkmcnt(0)
	v_mfma_scale_f32_16x16x128_f8f6f4 v[158:161], v[18:25], v[180:187], v[158:161], v191, v191 op_sel_hi:[0,0,0]
	v_mfma_scale_f32_16x16x128_f8f6f4 v[154:157], v[26:33], v[180:187], v[154:157], v191, v191 op_sel_hi:[0,0,0]
	v_mfma_scale_f32_16x16x128_f8f6f4 v[142:145], v[18:25], v[206:213], v[142:145], v191, v191 op_sel_hi:[0,0,0]
	v_mfma_scale_f32_16x16x128_f8f6f4 v[138:141], v[26:33], v[206:213], v[138:141], v191, v191 op_sel_hi:[0,0,0]
	v_mfma_scale_f32_16x16x128_f8f6f4 v[126:129], v[18:25], v[214:221], v[126:129], v191, v191 op_sel_hi:[0,0,0]
	v_mfma_scale_f32_16x16x128_f8f6f4 v[122:125], v[26:33], v[214:221], v[122:125], v191, v191 op_sel_hi:[0,0,0]
	v_mfma_scale_f32_16x16x128_f8f6f4 v[110:113], v[18:25], v[234:241], v[110:113], v191, v191 op_sel_hi:[0,0,0]
	v_mfma_scale_f32_16x16x128_f8f6f4 v[106:109], v[26:33], v[234:241], v[106:109], v191, v191 op_sel_hi:[0,0,0]
	s_setprio 0
	s_setprio 1
	v_mfma_scale_f32_16x16x128_f8f6f4 v[150:153], v[2:9], v[180:187], v[150:153], v191, v191 op_sel_hi:[0,0,0]
	v_mfma_scale_f32_16x16x128_f8f6f4 v[146:149], v[10:17], v[180:187], v[146:149], v191, v191 op_sel_hi:[0,0,0]
	v_mfma_scale_f32_16x16x128_f8f6f4 v[134:137], v[2:9], v[206:213], v[134:137], v191, v191 op_sel_hi:[0,0,0]
	v_mfma_scale_f32_16x16x128_f8f6f4 v[130:133], v[10:17], v[206:213], v[130:133], v191, v191 op_sel_hi:[0,0,0]
	v_mfma_scale_f32_16x16x128_f8f6f4 v[118:121], v[2:9], v[214:221], v[118:121], v191, v191 op_sel_hi:[0,0,0]
	v_mfma_scale_f32_16x16x128_f8f6f4 v[114:117], v[10:17], v[214:221], v[114:117], v191, v191 op_sel_hi:[0,0,0]
	v_mfma_scale_f32_16x16x128_f8f6f4 v[102:105], v[2:9], v[234:241], v[102:105], v191, v191 op_sel_hi:[0,0,0]
	v_mfma_scale_f32_16x16x128_f8f6f4 v[98:101], v[10:17], v[234:241], v[98:101], v191, v191 op_sel_hi:[0,0,0]
	s_setprio 0
	s_barrier
	s_add_i32 s4, s4, s92
	v_lshl_add_u64 v[180:181], s[36:37], 0, v[162:163]
	s_mov_b32 m0, s4
	ds_read_b128 v[206:209], v201 offset:16384
	ds_read_b128 v[210:213], v201 offset:17408
	ds_read_b128 v[214:217], v201 offset:18432
	ds_read_b128 v[218:221], v201 offset:19456
	ds_read_b128 v[234:237], v201 offset:20480
	ds_read_b128 v[238:241], v201 offset:21504
	ds_read_b128 v[242:245], v201 offset:22528
	ds_read_b128 v[246:249], v201 offset:23552
	global_load_lds_dwordx4 v[180:181], off
	s_add_i32 m0, s4, 0x2000
	s_add_u32 s86, s36, 0x20000
	v_lshl_add_u64 v[182:183], s[36:37], 0, v[164:165]
	s_addc_u32 s87, s37, 0
	s_add_i32 s4, s69, s92
	global_load_lds_dwordx4 v[182:183], off
	v_lshl_add_u64 v[184:185], s[86:87], 0, v[162:163]
	s_mov_b32 m0, s4
	v_cndmask_b32_e32 v0, v168, v202, vcc
	global_load_lds_dwordx4 v[184:185], off
	v_lshl_add_u64 v[184:185], s[86:87], 0, v[164:165]
	s_add_i32 m0, s4, 0x2000
	v_lshl_add_u64 v[186:187], s[70:71], 0, v[0:1]
	global_load_lds_dwordx4 v[184:185], off
	s_mov_b32 m0, s93
	v_cndmask_b32_e32 v184, v170, v203, vcc
	global_load_lds_dwordx4 v0, s[70:71]
	s_mov_b32 m0, s79
	v_mov_b32_e32 v185, v1
	global_load_lds_dwordx4 v184, s[70:71]
	s_waitcnt vmcnt(8)
	s_waitcnt lgkmcnt(0)
	v_lshl_add_u64 v[184:185], s[70:71], 0, v[184:185]
	s_barrier
	s_setprio 1
	s_waitcnt lgkmcnt(0)
	v_mfma_scale_f32_16x16x128_f8f6f4 v[94:97], v[18:25], v[206:213], v[94:97], v191, v191 op_sel_hi:[0,0,0]
	v_mfma_scale_f32_16x16x128_f8f6f4 v[90:93], v[26:33], v[206:213], v[90:93], v191, v191 op_sel_hi:[0,0,0]
	v_mfma_scale_f32_16x16x128_f8f6f4 v[70:73], v[18:25], v[214:221], v[70:73], v191, v191 op_sel_hi:[0,0,0]
	v_mfma_scale_f32_16x16x128_f8f6f4 v[66:69], v[26:33], v[214:221], v[66:69], v191, v191 op_sel_hi:[0,0,0]
	v_mfma_scale_f32_16x16x128_f8f6f4 v[54:57], v[18:25], v[234:241], v[54:57], v191, v191 op_sel_hi:[0,0,0]
	v_mfma_scale_f32_16x16x128_f8f6f4 v[50:53], v[26:33], v[234:241], v[50:53], v191, v191 op_sel_hi:[0,0,0]
	v_mfma_scale_f32_16x16x128_f8f6f4 v[38:41], v[18:25], v[242:249], v[38:41], v191, v191 op_sel_hi:[0,0,0]
	v_mfma_scale_f32_16x16x128_f8f6f4 v[34:37], v[26:33], v[242:249], v[34:37], v191, v191 op_sel_hi:[0,0,0]
	s_setprio 0
	s_setprio 1
	v_mfma_scale_f32_16x16x128_f8f6f4 v[86:89], v[2:9], v[206:213], v[86:89], v191, v191 op_sel_hi:[0,0,0]
	v_mfma_scale_f32_16x16x128_f8f6f4 v[82:85], v[10:17], v[206:213], v[82:85], v191, v191 op_sel_hi:[0,0,0]
	v_mfma_scale_f32_16x16x128_f8f6f4 v[78:81], v[2:9], v[214:221], v[78:81], v191, v191 op_sel_hi:[0,0,0]
	v_mfma_scale_f32_16x16x128_f8f6f4 v[74:77], v[10:17], v[214:221], v[74:77], v191, v191 op_sel_hi:[0,0,0]
	v_mfma_scale_f32_16x16x128_f8f6f4 v[62:65], v[2:9], v[234:241], v[62:65], v191, v191 op_sel_hi:[0,0,0]
	v_mfma_scale_f32_16x16x128_f8f6f4 v[58:61], v[10:17], v[234:241], v[58:61], v191, v191 op_sel_hi:[0,0,0]
	v_mfma_scale_f32_16x16x128_f8f6f4 v[46:49], v[2:9], v[242:249], v[46:49], v191, v191 op_sel_hi:[0,0,0]
	v_mfma_scale_f32_16x16x128_f8f6f4 v[42:45], v[10:17], v[242:249], v[42:45], v191, v191 op_sel_hi:[0,0,0]
	s_setprio 0
	s_barrier
	s_add_i32 s4, 0, 0x18000
	v_add_u32_e32 v0, s4, v200
	s_add_i32 s69, 0, 0x1c000
	ds_read_b128 v[2:5], v0
	ds_read_b128 v[6:9], v0 offset:1024
	ds_read_b128 v[10:13], v0 offset:2048
	ds_read_b128 v[14:17], v0 offset:3072
	v_add_u32_e32 v0, s69, v200
	ds_read_b128 v[18:21], v0
	ds_read_b128 v[22:25], v0 offset:1024
	ds_read_b128 v[26:29], v0 offset:2048
	ds_read_b128 v[30:33], v0 offset:3072
	s_mov_b32 m0, s84
	v_cndmask_b32_e32 v0, v172, v204, vcc
	ds_read_b128 v[206:209], v201 offset:32768
	ds_read_b128 v[210:213], v201 offset:33792
	ds_read_b128 v[214:217], v201 offset:34816
	ds_read_b128 v[218:221], v201 offset:35840
	ds_read_b128 v[234:237], v201 offset:36864
	ds_read_b128 v[238:241], v201 offset:37888
	ds_read_b128 v[242:245], v201 offset:38912
	ds_read_b128 v[246:249], v201 offset:39936
	v_cndmask_b32_e32 v173, v174, v205, vcc
	global_load_lds_dwordx4 v0, s[70:71]
	s_mov_b32 m0, s85
	s_nop 0
	global_load_lds_dwordx4 v173, s[70:71]
	s_waitcnt vmcnt(8)
	s_waitcnt lgkmcnt(0)
	s_barrier
	s_setprio 1
	s_waitcnt lgkmcnt(0)
	v_mfma_scale_f32_16x16x128_f8f6f4 v[158:161], v[2:9], v[206:213], v[158:161], v191, v191 op_sel_hi:[0,0,0]
	v_mfma_scale_f32_16x16x128_f8f6f4 v[154:157], v[10:17], v[206:213], v[154:157], v191, v191 op_sel_hi:[0,0,0]
	v_mfma_scale_f32_16x16x128_f8f6f4 v[142:145], v[2:9], v[214:221], v[142:145], v191, v191 op_sel_hi:[0,0,0]
	v_mfma_scale_f32_16x16x128_f8f6f4 v[138:141], v[10:17], v[214:221], v[138:141], v191, v191 op_sel_hi:[0,0,0]
	v_mfma_scale_f32_16x16x128_f8f6f4 v[126:129], v[2:9], v[234:241], v[126:129], v191, v191 op_sel_hi:[0,0,0]
	v_mfma_scale_f32_16x16x128_f8f6f4 v[122:125], v[10:17], v[234:241], v[122:125], v191, v191 op_sel_hi:[0,0,0]
	v_mfma_scale_f32_16x16x128_f8f6f4 v[110:113], v[2:9], v[242:249], v[110:113], v191, v191 op_sel_hi:[0,0,0]
	v_mfma_scale_f32_16x16x128_f8f6f4 v[106:109], v[10:17], v[242:249], v[106:109], v191, v191 op_sel_hi:[0,0,0]
	s_setprio 0
	s_setprio 1
	v_mfma_scale_f32_16x16x128_f8f6f4 v[150:153], v[18:25], v[206:213], v[150:153], v191, v191 op_sel_hi:[0,0,0]
	v_mfma_scale_f32_16x16x128_f8f6f4 v[146:149], v[26:33], v[206:213], v[146:149], v191, v191 op_sel_hi:[0,0,0]
	v_mfma_scale_f32_16x16x128_f8f6f4 v[134:137], v[18:25], v[214:221], v[134:137], v191, v191 op_sel_hi:[0,0,0]
	v_mfma_scale_f32_16x16x128_f8f6f4 v[130:133], v[26:33], v[214:221], v[130:133], v191, v191 op_sel_hi:[0,0,0]
	v_mfma_scale_f32_16x16x128_f8f6f4 v[118:121], v[18:25], v[234:241], v[118:121], v191, v191 op_sel_hi:[0,0,0]
	v_mfma_scale_f32_16x16x128_f8f6f4 v[114:117], v[26:33], v[234:241], v[114:117], v191, v191 op_sel_hi:[0,0,0]
	v_mfma_scale_f32_16x16x128_f8f6f4 v[102:105], v[18:25], v[242:249], v[102:105], v191, v191 op_sel_hi:[0,0,0]
	v_mfma_scale_f32_16x16x128_f8f6f4 v[98:101], v[26:33], v[242:249], v[98:101], v191, v191 op_sel_hi:[0,0,0]
	s_setprio 0
	s_barrier
	s_add_i32 s4, s4, s92
	v_lshl_add_u64 v[180:181], v[180:181], 0, s[22:23]
	s_mov_b32 m0, s4
	ds_read_b128 v[206:209], v201 offset:49152
	ds_read_b128 v[210:213], v201 offset:50176
	ds_read_b128 v[214:217], v201 offset:51200
	ds_read_b128 v[218:221], v201 offset:52224
	ds_read_b128 v[234:237], v201 offset:53248
	ds_read_b128 v[238:241], v201 offset:54272
	ds_read_b128 v[242:245], v201 offset:55296
	ds_read_b128 v[246:249], v201 offset:56320
	global_load_lds_dwordx4 v[180:181], off
	s_add_i32 m0, s4, 0x2000
	s_add_u32 s36, s36, 0x20080
	v_lshl_add_u64 v[180:181], v[182:183], 0, s[22:23]
	s_addc_u32 s37, s37, 0
	s_add_i32 s4, s69, s92
	global_load_lds_dwordx4 v[180:181], off
	v_lshl_add_u64 v[180:181], s[36:37], 0, v[162:163]
	s_mov_b32 m0, s4
	s_nop 0
	global_load_lds_dwordx4 v[180:181], off
	v_lshl_add_u64 v[180:181], s[36:37], 0, v[164:165]
	s_add_i32 m0, s4, 0x2000
	s_nop 0
	global_load_lds_dwordx4 v[180:181], off
	v_lshl_add_u64 v[180:181], v[186:187], 0, s[22:23]
	s_mov_b32 m0, s15
	s_nop 0
	global_load_lds_dwordx4 v[180:181], off
	v_lshl_add_u64 v[180:181], v[184:185], 0, s[22:23]
	s_mov_b32 m0, s16
	s_nop 0
	global_load_lds_dwordx4 v[180:181], off
	s_waitcnt vmcnt(8)
	s_waitcnt lgkmcnt(0)
	s_barrier
	s_setprio 1
	s_waitcnt lgkmcnt(0)
	v_mfma_scale_f32_16x16x128_f8f6f4 v[94:97], v[2:9], v[206:213], v[94:97], v191, v191 op_sel_hi:[0,0,0]
	v_mfma_scale_f32_16x16x128_f8f6f4 v[90:93], v[10:17], v[206:213], v[90:93], v191, v191 op_sel_hi:[0,0,0]
	v_mfma_scale_f32_16x16x128_f8f6f4 v[70:73], v[2:9], v[214:221], v[70:73], v191, v191 op_sel_hi:[0,0,0]
	v_mfma_scale_f32_16x16x128_f8f6f4 v[66:69], v[10:17], v[214:221], v[66:69], v191, v191 op_sel_hi:[0,0,0]
	v_mfma_scale_f32_16x16x128_f8f6f4 v[54:57], v[2:9], v[234:241], v[54:57], v191, v191 op_sel_hi:[0,0,0]
	v_mfma_scale_f32_16x16x128_f8f6f4 v[50:53], v[10:17], v[234:241], v[50:53], v191, v191 op_sel_hi:[0,0,0]
	v_mfma_scale_f32_16x16x128_f8f6f4 v[38:41], v[2:9], v[242:249], v[38:41], v191, v191 op_sel_hi:[0,0,0]
	v_mfma_scale_f32_16x16x128_f8f6f4 v[34:37], v[10:17], v[242:249], v[34:37], v191, v191 op_sel_hi:[0,0,0]
	s_setprio 0
	s_setprio 1
	v_mfma_scale_f32_16x16x128_f8f6f4 v[86:89], v[18:25], v[206:213], v[86:89], v191, v191 op_sel_hi:[0,0,0]
	v_mfma_scale_f32_16x16x128_f8f6f4 v[82:85], v[26:33], v[206:213], v[82:85], v191, v191 op_sel_hi:[0,0,0]
	v_mfma_scale_f32_16x16x128_f8f6f4 v[78:81], v[18:25], v[214:221], v[78:81], v191, v191 op_sel_hi:[0,0,0]
	v_mfma_scale_f32_16x16x128_f8f6f4 v[74:77], v[26:33], v[214:221], v[74:77], v191, v191 op_sel_hi:[0,0,0]
	v_mfma_scale_f32_16x16x128_f8f6f4 v[62:65], v[18:25], v[234:241], v[62:65], v191, v191 op_sel_hi:[0,0,0]
	v_mfma_scale_f32_16x16x128_f8f6f4 v[58:61], v[26:33], v[234:241], v[58:61], v191, v191 op_sel_hi:[0,0,0]
	v_mfma_scale_f32_16x16x128_f8f6f4 v[46:49], v[18:25], v[242:249], v[46:49], v191, v191 op_sel_hi:[0,0,0]
	v_mfma_scale_f32_16x16x128_f8f6f4 v[42:45], v[26:33], v[242:249], v[42:45], v191, v191 op_sel_hi:[0,0,0]
	s_setprio 0
	s_barrier
	s_add_i32 s67, s67, 2
	s_add_u32 s26, s26, 0x100
	s_addc_u32 s27, s27, 0
	s_cmp_gt_u32 s67, 5
	s_cbranch_scc0 .LBB0_249
	s_ashr_i32 s69, s68, 31
	s_lshl_b32 s66, s66, 7
	s_lshl_b64 s[26:27], s[68:69], 13
	v_or_b32_e32 v2, s66, v169
	s_add_u32 s26, s5, s26
	s_addc_u32 s27, s14, s27
	v_ashrrev_i32_e32 v3, 31, v2
	v_lshl_add_u64 v[6:7], v[2:3], 2, s[26:27]
	s_mov_b64 s[26:27], 0x1000
	v_lshl_add_u64 v[14:15], v[6:7], 0, s[26:27]
	global_load_dwordx4 v[2:5], v[6:7], off offset:16
	global_load_dwordx4 v[10:13], v[6:7], off
	v_add_co_u32_e32 v6, vcc, s9, v6
	v_lshl_add_u32 v22, s75, 8, v171
	s_nop 0
	v_addc_co_u32_e32 v7, vcc, 0, v7, vcc
	global_load_dwordx4 v[6:9], v[6:7], off
	s_nop 0
	global_load_dwordx4 v[14:17], v[14:15], off offset:16
	s_and_b64 vcc, exec, s[58:59]
	s_cbranch_vccz .LBB0_252
	s_barrier
.LBB0_252:
	s_nop 15
	s_nop 15
	v_ashrrev_i32_e32 v23, 31, v22
	s_ashr_i32 s67, s66, 31
	s_mov_b64 s[26:27], -1
	s_and_b64 vcc, exec, s[38:39]
	s_waitcnt vmcnt(0)
	v_pk_fma_f32 v[26:27], v[154:155], s[24:25], v[2:3] op_sel_hi:[1,0,1]
	v_pk_fma_f32 v[18:19], v[160:161], s[24:25], v[12:13] op_sel_hi:[1,0,1]
	v_pk_fma_f32 v[20:21], v[158:159], s[24:25], v[10:11] op_sel_hi:[1,0,1]
	v_min_f32_e32 v18, 0x40e00000, v18
	v_min_f32_e32 v20, 0x40e00000, v20
	v_min_f32_e32 v21, 0x40e00000, v21
	v_pk_fma_f32 v[30:31], v[150:151], s[24:25], v[6:7] op_sel_hi:[1,0,1]
	v_min_f32_e32 v19, 0x40e00000, v19
	v_med3_f32 v30, v30, s19, v227
	v_med3_f32 v31, v31, s19, v227
	v_pk_add_f32 v[30:31], v[30:31], 1.0 op_sel_hi:[1,0]
	v_pk_fma_f32 v[32:33], v[148:149], s[24:25], v[16:17] op_sel_hi:[1,0,1]
	v_pk_mul_f32 v[148:149], v[20:21], s[28:29] op_sel_hi:[1,0]
	v_pk_mul_f32 v[20:21], v[20:21], v[30:31]
	v_pk_mul_f32 v[30:31], v[18:19], s[28:29] op_sel_hi:[1,0]
	v_pk_fma_f32 v[24:25], v[152:153], s[24:25], v[8:9] op_sel_hi:[1,0,1]
	v_exp_f32_e32 v30, v30
	v_exp_f32_e32 v31, v31
	v_med3_f32 v24, v24, s19, v227
	v_med3_f32 v25, v25, s19, v227
	v_pk_add_f32 v[24:25], v[24:25], 1.0 op_sel_hi:[1,0]
	v_pk_add_f32 v[30:31], v[30:31], 1.0 op_sel_hi:[1,0]
	v_pk_mul_f32 v[18:19], v[18:19], v[24:25]
	v_rcp_f32_e32 v30, v30
	v_rcp_f32_e32 v31, v31
	v_pk_fma_f32 v[146:147], v[146:147], s[24:25], v[14:15] op_sel_hi:[1,0,1]
	v_pk_fma_f32 v[28:29], v[156:157], s[24:25], v[4:5] op_sel_hi:[1,0,1]
	v_exp_f32_e32 v148, v148
	v_pk_mul_f32 v[24:25], v[18:19], v[30:31]
	v_min_f32_e32 v18, 0x40e00000, v26
	v_min_f32_e32 v19, 0x40e00000, v27
	v_pk_mul_f32 v[30:31], v[18:19], s[28:29] op_sel_hi:[1,0]
	v_med3_f32 v26, v146, s19, v227
	v_exp_f32_e32 v30, v30
	v_exp_f32_e32 v31, v31
	v_med3_f32 v27, v147, s19, v227
	v_pk_add_f32 v[26:27], v[26:27], 1.0 op_sel_hi:[1,0]
	v_exp_f32_e32 v149, v149
	v_pk_add_f32 v[30:31], v[30:31], 1.0 op_sel_hi:[1,0]
	v_pk_mul_f32 v[18:19], v[18:19], v[26:27]
	v_rcp_f32_e32 v30, v30
	v_rcp_f32_e32 v31, v31
	v_pk_add_f32 v[148:149], v[148:149], 1.0 op_sel_hi:[1,0]
	v_pk_fma_f32 v[134:135], v[134:135], s[24:25], v[6:7] op_sel_hi:[1,0,1]
	v_rcp_f32_e32 v148, v148
	v_pk_mul_f32 v[26:27], v[18:19], v[30:31]
	v_min_f32_e32 v18, 0x40e00000, v28
	v_min_f32_e32 v19, 0x40e00000, v29
	v_pk_mul_f32 v[30:31], v[18:19], s[28:29] op_sel_hi:[1,0]
	v_rcp_f32_e32 v149, v149
	v_exp_f32_e32 v30, v30
	v_exp_f32_e32 v31, v31
	v_med3_f32 v28, v32, s19, v227
	v_med3_f32 v29, v33, s19, v227
	v_pk_add_f32 v[28:29], v[28:29], 1.0 op_sel_hi:[1,0]
	v_pk_add_f32 v[30:31], v[30:31], 1.0 op_sel_hi:[1,0]
	v_pk_mul_f32 v[18:19], v[18:19], v[28:29]
	v_rcp_f32_e32 v30, v30
	v_rcp_f32_e32 v31, v31
	v_pk_mul_f32 v[20:21], v[20:21], v[148:149]
	v_pk_fma_f32 v[32:33], v[136:137], s[24:25], v[8:9] op_sel_hi:[1,0,1]
	v_pk_fma_f32 v[142:143], v[142:143], s[24:25], v[10:11] op_sel_hi:[1,0,1]
	v_pk_mul_f32 v[28:29], v[18:19], v[30:31]
	v_mov_b32_e32 v19, v1
	v_mov_b32_e32 v18, v1
	v_cvt_pk_fp8_f32 v19, v26, v27
	v_cvt_pk_fp8_f32 v18, v20, v21
	v_pk_fma_f32 v[30:31], v[144:145], s[24:25], v[12:13] op_sel_hi:[1,0,1]
	v_pk_fma_f32 v[20:21], v[140:141], s[24:25], v[4:5] op_sel_hi:[1,0,1]
	v_cvt_pk_fp8_f32 v19, v28, v29 op_sel:[0,0,1]
	v_pk_fma_f32 v[28:29], v[130:131], s[24:25], v[14:15] op_sel_hi:[1,0,1]
	v_cvt_pk_fp8_f32 v18, v24, v25 op_sel:[0,0,1]
	v_pk_fma_f32 v[26:27], v[138:139], s[24:25], v[2:3] op_sel_hi:[1,0,1]
	v_pk_fma_f32 v[24:25], v[132:133], s[24:25], v[16:17] op_sel_hi:[1,0,1]
	v_med3_f32 v132, v134, s19, v227
	v_med3_f32 v133, v135, s19, v227
	v_med3_f32 v32, v32, s19, v227
	v_med3_f32 v33, v33, s19, v227
	v_med3_f32 v28, v28, s19, v227
	v_med3_f32 v29, v29, s19, v227
	v_min_f32_e32 v130, 0x40e00000, v142
	v_min_f32_e32 v131, 0x40e00000, v143
	v_pk_add_f32 v[132:133], v[132:133], 1.0 op_sel_hi:[1,0]
	v_min_f32_e32 v30, 0x40e00000, v30
	v_min_f32_e32 v31, 0x40e00000, v31
	v_pk_add_f32 v[32:33], v[32:33], 1.0 op_sel_hi:[1,0]
	v_min_f32_e32 v26, 0x40e00000, v26
	v_min_f32_e32 v27, 0x40e00000, v27
	v_pk_add_f32 v[28:29], v[28:29], 1.0 op_sel_hi:[1,0]
	v_min_f32_e32 v20, 0x40e00000, v20
	v_min_f32_e32 v21, 0x40e00000, v21
	v_pk_mul_f32 v[134:135], v[130:131], s[28:29] op_sel_hi:[1,0]
	v_pk_mul_f32 v[130:131], v[130:131], v[132:133]
	v_pk_mul_f32 v[132:133], v[30:31], s[28:29] op_sel_hi:[1,0]
	v_pk_mul_f32 v[30:31], v[30:31], v[32:33]
	v_pk_mul_f32 v[32:33], v[26:27], s[28:29] op_sel_hi:[1,0]
	v_pk_mul_f32 v[26:27], v[26:27], v[28:29]
	v_pk_mul_f32 v[28:29], v[20:21], s[28:29] op_sel_hi:[1,0]
	v_exp_f32_e32 v134, v134
	v_exp_f32_e32 v135, v135
	v_exp_f32_e32 v32, v32
	v_exp_f32_e32 v33, v33
	v_exp_f32_e32 v28, v28
	v_exp_f32_e32 v29, v29
	v_pk_add_f32 v[134:135], v[134:135], 1.0 op_sel_hi:[1,0]
	v_exp_f32_e32 v132, v132
	v_exp_f32_e32 v133, v133
	v_pk_add_f32 v[32:33], v[32:33], 1.0 op_sel_hi:[1,0]
	v_pk_add_f32 v[28:29], v[28:29], 1.0 op_sel_hi:[1,0]
	v_rcp_f32_e32 v134, v134
	v_rcp_f32_e32 v135, v135
	v_rcp_f32_e32 v32, v32
	v_rcp_f32_e32 v33, v33
	v_rcp_f32_e32 v28, v28
	v_rcp_f32_e32 v29, v29
	v_med3_f32 v24, v24, s19, v227
	v_med3_f32 v25, v25, s19, v227
	v_pk_add_f32 v[24:25], v[24:25], 1.0 op_sel_hi:[1,0]
	v_pk_add_f32 v[132:133], v[132:133], 1.0 op_sel_hi:[1,0]
	v_pk_mul_f32 v[20:21], v[20:21], v[24:25]
	v_pk_mul_f32 v[130:131], v[130:131], v[134:135]
	v_rcp_f32_e32 v132, v132
	v_rcp_f32_e32 v133, v133
	v_pk_mul_f32 v[26:27], v[26:27], v[32:33]
	v_pk_mul_f32 v[24:25], v[20:21], v[28:29]
	v_mov_b32_e32 v20, v1
	v_mov_b32_e32 v21, v1
	v_cvt_pk_fp8_f32 v20, v130, v131
	v_cvt_pk_fp8_f32 v21, v26, v27
	v_pk_mul_f32 v[30:31], v[30:31], v[132:133]
	v_pk_fma_f32 v[32:33], v[116:117], s[24:25], v[16:17] op_sel_hi:[1,0,1]
	v_cvt_pk_fp8_f32 v20, v30, v31 op_sel:[0,0,1]
	v_cvt_pk_fp8_f32 v21, v24, v25 op_sel:[0,0,1]
	v_lshlrev_b64 v[24:25], 10, v[22:23]
	v_lshl_add_u64 v[24:25], s[50:51], 0, v[24:25]
	v_lshl_add_u64 v[24:25], v[24:25], 0, s[66:67]
	v_lshl_add_u64 v[24:25], v[24:25], 0, s[52:53]
	v_permlane16_swap_b32_e32 v18, v20
	v_permlane16_swap_b32_e32 v19, v21
	v_lshl_add_u64 v[24:25], v[24:25], 0, v[166:167]
	v_pk_fma_f32 v[30:31], v[118:119], s[24:25], v[6:7] op_sel_hi:[1,0,1]
	global_store_dwordx4 v[24:25], v[18:21], off
	v_med3_f32 v30, v30, s19, v227
	v_med3_f32 v31, v31, s19, v227
	v_pk_fma_f32 v[18:19], v[128:129], s[24:25], v[12:13] op_sel_hi:[1,0,1]
	v_pk_fma_f32 v[20:21], v[126:127], s[24:25], v[10:11] op_sel_hi:[1,0,1]
	v_pk_add_f32 v[30:31], v[30:31], 1.0 op_sel_hi:[1,0]
	v_min_f32_e32 v20, 0x40e00000, v20
	v_min_f32_e32 v21, 0x40e00000, v21
	v_min_f32_e32 v18, 0x40e00000, v18
	v_min_f32_e32 v19, 0x40e00000, v19
	v_pk_mul_f32 v[116:117], v[20:21], s[28:29] op_sel_hi:[1,0]
	v_pk_mul_f32 v[20:21], v[20:21], v[30:31]
	v_pk_mul_f32 v[30:31], v[18:19], s[28:29] op_sel_hi:[1,0]
	v_pk_fma_f32 v[28:29], v[120:121], s[24:25], v[8:9] op_sel_hi:[1,0,1]
	v_exp_f32_e32 v30, v30
	v_exp_f32_e32 v31, v31
	v_med3_f32 v28, v28, s19, v227
	v_med3_f32 v29, v29, s19, v227
	v_pk_add_f32 v[28:29], v[28:29], 1.0 op_sel_hi:[1,0]
	v_pk_add_f32 v[30:31], v[30:31], 1.0 op_sel_hi:[1,0]
	v_pk_fma_f32 v[26:27], v[122:123], s[24:25], v[2:3] op_sel_hi:[1,0,1]
	v_rcp_f32_e32 v30, v30
	v_rcp_f32_e32 v31, v31
	v_pk_mul_f32 v[18:19], v[18:19], v[28:29]
	v_pk_fma_f32 v[114:115], v[114:115], s[24:25], v[14:15] op_sel_hi:[1,0,1]
	v_pk_fma_f32 v[24:25], v[124:125], s[24:25], v[4:5] op_sel_hi:[1,0,1]
	v_pk_mul_f32 v[28:29], v[18:19], v[30:31]
	v_min_f32_e32 v18, 0x40e00000, v26
	v_min_f32_e32 v19, 0x40e00000, v27
	v_pk_mul_f32 v[30:31], v[18:19], s[28:29] op_sel_hi:[1,0]
	v_med3_f32 v26, v114, s19, v227
	v_exp_f32_e32 v30, v30
	v_exp_f32_e32 v31, v31
	v_med3_f32 v27, v115, s19, v227
	v_pk_add_f32 v[26:27], v[26:27], 1.0 op_sel_hi:[1,0]
	v_exp_f32_e32 v116, v116
	v_pk_add_f32 v[30:31], v[30:31], 1.0 op_sel_hi:[1,0]
	v_pk_mul_f32 v[18:19], v[18:19], v[26:27]
	v_rcp_f32_e32 v30, v30
	v_rcp_f32_e32 v31, v31
	v_exp_f32_e32 v117, v117
	v_pk_fma_f32 v[98:99], v[98:99], s[24:25], v[14:15] op_sel_hi:[1,0,1]
	v_pk_fma_f32 v[100:101], v[100:101], s[24:25], v[16:17] op_sel_hi:[1,0,1]
	v_pk_mul_f32 v[26:27], v[18:19], v[30:31]
	v_min_f32_e32 v18, 0x40e00000, v24
	v_min_f32_e32 v19, 0x40e00000, v25
	v_pk_mul_f32 v[30:31], v[18:19], s[28:29] op_sel_hi:[1,0]
	v_med3_f32 v24, v32, s19, v227
	v_exp_f32_e32 v30, v30
	v_exp_f32_e32 v31, v31
	v_med3_f32 v25, v33, s19, v227
	v_pk_add_f32 v[24:25], v[24:25], 1.0 op_sel_hi:[1,0]
	v_pk_add_f32 v[116:117], v[116:117], 1.0 op_sel_hi:[1,0]
	v_pk_add_f32 v[30:31], v[30:31], 1.0 op_sel_hi:[1,0]
	v_pk_mul_f32 v[18:19], v[18:19], v[24:25]
	v_rcp_f32_e32 v30, v30
	v_rcp_f32_e32 v31, v31
	v_rcp_f32_e32 v116, v116
	v_rcp_f32_e32 v117, v117
	v_pk_fma_f32 v[32:33], v[102:103], s[24:25], v[6:7] op_sel_hi:[1,0,1]
	v_pk_mul_f32 v[24:25], v[18:19], v[30:31]
	v_mov_b32_e32 v19, v1
	v_cvt_pk_fp8_f32 v19, v26, v27
	v_pk_mul_f32 v[20:21], v[20:21], v[116:117]
	v_mov_b32_e32 v18, v1
	v_cvt_pk_fp8_f32 v18, v20, v21
	v_cvt_pk_fp8_f32 v19, v24, v25 op_sel:[0,0,1]
	v_pk_fma_f32 v[20:21], v[112:113], s[24:25], v[12:13] op_sel_hi:[1,0,1]
	v_pk_fma_f32 v[24:25], v[110:111], s[24:25], v[10:11] op_sel_hi:[1,0,1]
	v_med3_f32 v32, v32, s19, v227
	v_med3_f32 v33, v33, s19, v227
	v_min_f32_e32 v24, 0x40e00000, v24
	v_min_f32_e32 v25, 0x40e00000, v25
	v_pk_add_f32 v[32:33], v[32:33], 1.0 op_sel_hi:[1,0]
	v_min_f32_e32 v20, 0x40e00000, v20
	v_min_f32_e32 v21, 0x40e00000, v21
	v_pk_mul_f32 v[102:103], v[24:25], s[28:29] op_sel_hi:[1,0]
	v_pk_mul_f32 v[24:25], v[24:25], v[32:33]
	v_pk_mul_f32 v[32:33], v[20:21], s[28:29] op_sel_hi:[1,0]
	v_pk_fma_f32 v[30:31], v[104:105], s[24:25], v[8:9] op_sel_hi:[1,0,1]
	v_exp_f32_e32 v32, v32
	v_exp_f32_e32 v33, v33
	v_med3_f32 v30, v30, s19, v227
	v_med3_f32 v31, v31, s19, v227
	v_pk_add_f32 v[30:31], v[30:31], 1.0 op_sel_hi:[1,0]
	v_pk_add_f32 v[32:33], v[32:33], 1.0 op_sel_hi:[1,0]
	v_cvt_pk_fp8_f32 v18, v28, v29 op_sel:[0,0,1]
	v_rcp_f32_e32 v32, v32
	v_rcp_f32_e32 v33, v33
	v_pk_fma_f32 v[28:29], v[106:107], s[24:25], v[2:3] op_sel_hi:[1,0,1]
	v_pk_mul_f32 v[20:21], v[20:21], v[30:31]
	v_pk_fma_f32 v[26:27], v[108:109], s[24:25], v[4:5] op_sel_hi:[1,0,1]
	v_pk_mul_f32 v[30:31], v[20:21], v[32:33]
	v_min_f32_e32 v20, 0x40e00000, v28
	v_min_f32_e32 v21, 0x40e00000, v29
	v_pk_mul_f32 v[32:33], v[20:21], s[28:29] op_sel_hi:[1,0]
	v_med3_f32 v28, v98, s19, v227
	v_exp_f32_e32 v32, v32
	v_exp_f32_e32 v33, v33
	v_med3_f32 v29, v99, s19, v227
	v_pk_add_f32 v[28:29], v[28:29], 1.0 op_sel_hi:[1,0]
	v_exp_f32_e32 v102, v102
	v_pk_add_f32 v[32:33], v[32:33], 1.0 op_sel_hi:[1,0]
	v_pk_mul_f32 v[20:21], v[20:21], v[28:29]
	v_rcp_f32_e32 v32, v32
	v_rcp_f32_e32 v33, v33
	v_exp_f32_e32 v103, v103
	v_pk_fma_f32 v[82:83], v[82:83], s[24:25], v[14:15] op_sel_hi:[1,0,1]
	v_pk_fma_f32 v[84:85], v[84:85], s[24:25], v[16:17] op_sel_hi:[1,0,1]
	v_pk_mul_f32 v[28:29], v[20:21], v[32:33]
	v_min_f32_e32 v20, 0x40e00000, v26
	v_min_f32_e32 v21, 0x40e00000, v27
	v_pk_mul_f32 v[32:33], v[20:21], s[28:29] op_sel_hi:[1,0]
	v_pk_add_f32 v[102:103], v[102:103], 1.0 op_sel_hi:[1,0]
	v_exp_f32_e32 v32, v32
	v_exp_f32_e32 v33, v33
	v_rcp_f32_e32 v102, v102
	v_rcp_f32_e32 v103, v103
	v_med3_f32 v26, v100, s19, v227
	v_pk_add_f32 v[32:33], v[32:33], 1.0 op_sel_hi:[1,0]
	v_med3_f32 v27, v101, s19, v227
	v_rcp_f32_e32 v32, v32
	v_rcp_f32_e32 v33, v33
	v_pk_add_f32 v[26:27], v[26:27], 1.0 op_sel_hi:[1,0]
	v_pk_mul_f32 v[24:25], v[24:25], v[102:103]
	v_pk_mul_f32 v[20:21], v[20:21], v[26:27]
	s_nop 0
	v_pk_mul_f32 v[26:27], v[20:21], v[32:33]
	v_mov_b32_e32 v20, v1
	v_mov_b32_e32 v21, v1
	v_cvt_pk_fp8_f32 v20, v24, v25
	v_cvt_pk_fp8_f32 v21, v28, v29
	v_or_b32_e32 v24, 32, v22
	v_ashrrev_i32_e32 v25, 31, v24
	v_cvt_pk_fp8_f32 v20, v30, v31 op_sel:[0,0,1]
	v_cvt_pk_fp8_f32 v21, v26, v27 op_sel:[0,0,1]
	v_lshlrev_b64 v[24:25], 10, v[24:25]
	v_lshl_add_u64 v[24:25], s[50:51], 0, v[24:25]
	v_lshl_add_u64 v[24:25], v[24:25], 0, s[66:67]
	v_lshl_add_u64 v[24:25], v[24:25], 0, s[52:53]
	v_permlane16_swap_b32_e32 v18, v20
	v_permlane16_swap_b32_e32 v19, v21
	v_lshl_add_u64 v[24:25], v[24:25], 0, v[166:167]
	v_pk_fma_f32 v[32:33], v[86:87], s[24:25], v[6:7] op_sel_hi:[1,0,1]
	global_store_dwordx4 v[24:25], v[18:21], off
	v_med3_f32 v32, v32, s19, v227
	v_med3_f32 v33, v33, s19, v227
	v_pk_fma_f32 v[18:19], v[96:97], s[24:25], v[12:13] op_sel_hi:[1,0,1]
	v_pk_fma_f32 v[20:21], v[94:95], s[24:25], v[10:11] op_sel_hi:[1,0,1]
	v_pk_add_f32 v[32:33], v[32:33], 1.0 op_sel_hi:[1,0]
	v_min_f32_e32 v20, 0x40e00000, v20
	v_min_f32_e32 v21, 0x40e00000, v21
	v_min_f32_e32 v18, 0x40e00000, v18
	v_min_f32_e32 v19, 0x40e00000, v19
	v_pk_mul_f32 v[86:87], v[20:21], s[28:29] op_sel_hi:[1,0]
	v_pk_mul_f32 v[20:21], v[20:21], v[32:33]
	v_pk_mul_f32 v[32:33], v[18:19], s[28:29] op_sel_hi:[1,0]
	v_pk_fma_f32 v[30:31], v[88:89], s[24:25], v[8:9] op_sel_hi:[1,0,1]
	v_exp_f32_e32 v32, v32
	v_exp_f32_e32 v33, v33
	v_med3_f32 v30, v30, s19, v227
	v_med3_f32 v31, v31, s19, v227
	v_pk_add_f32 v[30:31], v[30:31], 1.0 op_sel_hi:[1,0]
	v_pk_add_f32 v[32:33], v[32:33], 1.0 op_sel_hi:[1,0]
	v_pk_fma_f32 v[28:29], v[90:91], s[24:25], v[2:3] op_sel_hi:[1,0,1]
	v_rcp_f32_e32 v32, v32
	v_rcp_f32_e32 v33, v33
	v_pk_mul_f32 v[18:19], v[18:19], v[30:31]
	v_pk_fma_f32 v[26:27], v[92:93], s[24:25], v[4:5] op_sel_hi:[1,0,1]
	v_exp_f32_e32 v86, v86
	v_pk_mul_f32 v[30:31], v[18:19], v[32:33]
	v_min_f32_e32 v18, 0x40e00000, v28
	v_min_f32_e32 v19, 0x40e00000, v29
	v_pk_mul_f32 v[32:33], v[18:19], s[28:29] op_sel_hi:[1,0]
	v_med3_f32 v28, v82, s19, v227
	v_exp_f32_e32 v32, v32
	v_exp_f32_e32 v33, v33
	v_med3_f32 v29, v83, s19, v227
	v_pk_add_f32 v[28:29], v[28:29], 1.0 op_sel_hi:[1,0]
	v_exp_f32_e32 v87, v87
	v_pk_add_f32 v[32:33], v[32:33], 1.0 op_sel_hi:[1,0]
	v_pk_mul_f32 v[18:19], v[18:19], v[28:29]
	v_rcp_f32_e32 v32, v32
	v_rcp_f32_e32 v33, v33
	v_pk_add_f32 v[86:87], v[86:87], 1.0 op_sel_hi:[1,0]
	v_add_u32_e32 v24, 0x80, v22
	v_rcp_f32_e32 v86, v86
	v_pk_mul_f32 v[28:29], v[18:19], v[32:33]
	v_min_f32_e32 v18, 0x40e00000, v26
	v_min_f32_e32 v19, 0x40e00000, v27
	v_pk_mul_f32 v[32:33], v[18:19], s[28:29] op_sel_hi:[1,0]
	v_rcp_f32_e32 v87, v87
	v_exp_f32_e32 v32, v32
	v_exp_f32_e32 v33, v33
	v_med3_f32 v26, v84, s19, v227
	v_med3_f32 v27, v85, s19, v227
	v_pk_add_f32 v[26:27], v[26:27], 1.0 op_sel_hi:[1,0]
	v_pk_add_f32 v[32:33], v[32:33], 1.0 op_sel_hi:[1,0]
	v_pk_mul_f32 v[18:19], v[18:19], v[26:27]
	v_rcp_f32_e32 v32, v32
	v_rcp_f32_e32 v33, v33
	v_pk_mul_f32 v[20:21], v[20:21], v[86:87]
	v_ashrrev_i32_e32 v25, 31, v24
	v_lshlrev_b64 v[24:25], 10, v[24:25]
	v_pk_mul_f32 v[26:27], v[18:19], v[32:33]
	v_mov_b32_e32 v18, v1
	v_cvt_pk_fp8_f32 v18, v20, v21
	v_mov_b32_e32 v19, v1
	v_cvt_pk_fp8_f32 v19, v28, v29
	v_pk_fma_f32 v[20:21], v[72:73], s[24:25], v[12:13] op_sel_hi:[1,0,1]
	v_cvt_pk_fp8_f32 v18, v30, v31 op_sel:[0,0,1]
	v_pk_fma_f32 v[30:31], v[66:67], s[24:25], v[2:3] op_sel_hi:[1,0,1]
	v_pk_fma_f32 v[66:67], v[78:79], s[24:25], v[6:7] op_sel_hi:[1,0,1]
	v_cvt_pk_fp8_f32 v19, v26, v27 op_sel:[0,0,1]
	v_pk_fma_f32 v[26:27], v[70:71], s[24:25], v[10:11] op_sel_hi:[1,0,1]
	v_med3_f32 v66, v66, s19, v227
	v_med3_f32 v67, v67, s19, v227
	v_min_f32_e32 v26, 0x40e00000, v26
	v_min_f32_e32 v27, 0x40e00000, v27
	v_pk_add_f32 v[66:67], v[66:67], 1.0 op_sel_hi:[1,0]
	v_min_f32_e32 v20, 0x40e00000, v20
	v_min_f32_e32 v21, 0x40e00000, v21
	v_pk_mul_f32 v[72:73], v[26:27], s[28:29] op_sel_hi:[1,0]
	v_pk_mul_f32 v[26:27], v[26:27], v[66:67]
	v_pk_mul_f32 v[66:67], v[20:21], s[28:29] op_sel_hi:[1,0]
	v_pk_fma_f32 v[32:33], v[80:81], s[24:25], v[8:9] op_sel_hi:[1,0,1]
	v_exp_f32_e32 v66, v66
	v_exp_f32_e32 v67, v67
	v_med3_f32 v32, v32, s19, v227
	v_med3_f32 v33, v33, s19, v227
	v_pk_add_f32 v[32:33], v[32:33], 1.0 op_sel_hi:[1,0]
	v_pk_add_f32 v[66:67], v[66:67], 1.0 op_sel_hi:[1,0]
	v_pk_mul_f32 v[20:21], v[20:21], v[32:33]
	v_rcp_f32_e32 v66, v66
	v_rcp_f32_e32 v67, v67
	v_pk_fma_f32 v[70:71], v[74:75], s[24:25], v[14:15] op_sel_hi:[1,0,1]
	v_pk_fma_f32 v[28:29], v[68:69], s[24:25], v[4:5] op_sel_hi:[1,0,1]
	v_exp_f32_e32 v72, v72
	v_pk_mul_f32 v[32:33], v[20:21], v[66:67]
	v_min_f32_e32 v20, 0x40e00000, v30
	v_min_f32_e32 v21, 0x40e00000, v31
	v_pk_mul_f32 v[66:67], v[20:21], s[28:29] op_sel_hi:[1,0]
	v_med3_f32 v30, v70, s19, v227
	v_exp_f32_e32 v66, v66
	v_exp_f32_e32 v67, v67
	v_med3_f32 v31, v71, s19, v227
	v_pk_add_f32 v[30:31], v[30:31], 1.0 op_sel_hi:[1,0]
	v_exp_f32_e32 v73, v73
	v_pk_add_f32 v[66:67], v[66:67], 1.0 op_sel_hi:[1,0]
	v_pk_mul_f32 v[20:21], v[20:21], v[30:31]
	v_rcp_f32_e32 v66, v66
	v_rcp_f32_e32 v67, v67
	v_pk_add_f32 v[72:73], v[72:73], 1.0 op_sel_hi:[1,0]
	v_pk_fma_f32 v[68:69], v[76:77], s[24:25], v[16:17] op_sel_hi:[1,0,1]
	v_rcp_f32_e32 v72, v72
	v_pk_mul_f32 v[30:31], v[20:21], v[66:67]
	v_min_f32_e32 v20, 0x40e00000, v28
	v_min_f32_e32 v21, 0x40e00000, v29
	v_pk_mul_f32 v[66:67], v[20:21], s[28:29] op_sel_hi:[1,0]
	v_rcp_f32_e32 v73, v73
	v_exp_f32_e32 v66, v66
	v_exp_f32_e32 v67, v67
	v_med3_f32 v28, v68, s19, v227
	v_med3_f32 v29, v69, s19, v227
	v_pk_add_f32 v[28:29], v[28:29], 1.0 op_sel_hi:[1,0]
	v_pk_add_f32 v[66:67], v[66:67], 1.0 op_sel_hi:[1,0]
	v_pk_mul_f32 v[20:21], v[20:21], v[28:29]
	v_rcp_f32_e32 v66, v66
	v_rcp_f32_e32 v67, v67
	v_pk_mul_f32 v[26:27], v[26:27], v[72:73]
	v_lshl_add_u64 v[24:25], s[50:51], 0, v[24:25]
	v_lshl_add_u64 v[24:25], v[24:25], 0, s[66:67]
	v_pk_mul_f32 v[28:29], v[20:21], v[66:67]
	v_mov_b32_e32 v20, v1
	v_mov_b32_e32 v21, v1
	v_cvt_pk_fp8_f32 v20, v26, v27
	v_cvt_pk_fp8_f32 v21, v30, v31
	v_lshl_add_u64 v[24:25], v[24:25], 0, s[52:53]
	v_lshl_add_u64 v[24:25], v[24:25], 0, v[166:167]
	v_cvt_pk_fp8_f32 v20, v32, v33 op_sel:[0,0,1]
	v_cvt_pk_fp8_f32 v21, v28, v29 op_sel:[0,0,1]
	v_pk_fma_f32 v[30:31], v[62:63], s[24:25], v[6:7] op_sel_hi:[1,0,1]
	v_pk_fma_f32 v[28:29], v[64:65], s[24:25], v[8:9] op_sel_hi:[1,0,1]
	v_permlane16_swap_b32_e32 v18, v20
	v_permlane16_swap_b32_e32 v19, v21
	global_store_dwordx4 v[24:25], v[18:21], off
	v_med3_f32 v30, v30, s19, v227
	v_med3_f32 v31, v31, s19, v227
	v_pk_fma_f32 v[18:19], v[56:57], s[24:25], v[12:13] op_sel_hi:[1,0,1]
	v_pk_fma_f32 v[20:21], v[54:55], s[24:25], v[10:11] op_sel_hi:[1,0,1]
	v_pk_add_f32 v[30:31], v[30:31], 1.0 op_sel_hi:[1,0]
	v_min_f32_e32 v20, 0x40e00000, v20
	v_min_f32_e32 v21, 0x40e00000, v21
	v_min_f32_e32 v18, 0x40e00000, v18
	v_min_f32_e32 v19, 0x40e00000, v19
	v_pk_fma_f32 v[24:25], v[52:53], s[24:25], v[4:5] op_sel_hi:[1,0,1]
	v_pk_mul_f32 v[52:53], v[20:21], s[28:29] op_sel_hi:[1,0]
	v_pk_mul_f32 v[20:21], v[20:21], v[30:31]
	v_pk_mul_f32 v[30:31], v[18:19], s[28:29] op_sel_hi:[1,0]
	v_med3_f32 v28, v28, s19, v227
	v_exp_f32_e32 v30, v30
	v_exp_f32_e32 v31, v31
	v_med3_f32 v29, v29, s19, v227
	v_pk_add_f32 v[28:29], v[28:29], 1.0 op_sel_hi:[1,0]
	v_pk_fma_f32 v[26:27], v[50:51], s[24:25], v[2:3] op_sel_hi:[1,0,1]
	v_pk_add_f32 v[30:31], v[30:31], 1.0 op_sel_hi:[1,0]
	v_pk_mul_f32 v[18:19], v[18:19], v[28:29]
	v_rcp_f32_e32 v30, v30
	v_rcp_f32_e32 v31, v31
	v_pk_fma_f32 v[50:51], v[58:59], s[24:25], v[14:15] op_sel_hi:[1,0,1]
	v_exp_f32_e32 v52, v52
	v_exp_f32_e32 v53, v53
	v_pk_mul_f32 v[28:29], v[18:19], v[30:31]
	v_min_f32_e32 v18, 0x40e00000, v26
	v_min_f32_e32 v19, 0x40e00000, v27
	v_pk_mul_f32 v[30:31], v[18:19], s[28:29] op_sel_hi:[1,0]
	v_med3_f32 v26, v50, s19, v227
	v_exp_f32_e32 v30, v30
	v_exp_f32_e32 v31, v31
	v_med3_f32 v27, v51, s19, v227
	v_pk_add_f32 v[26:27], v[26:27], 1.0 op_sel_hi:[1,0]
	v_pk_add_f32 v[52:53], v[52:53], 1.0 op_sel_hi:[1,0]
	v_pk_add_f32 v[30:31], v[30:31], 1.0 op_sel_hi:[1,0]
	v_pk_mul_f32 v[18:19], v[18:19], v[26:27]
	v_rcp_f32_e32 v30, v30
	v_rcp_f32_e32 v31, v31
	v_pk_fma_f32 v[32:33], v[60:61], s[24:25], v[16:17] op_sel_hi:[1,0,1]
	v_rcp_f32_e32 v52, v52
	v_rcp_f32_e32 v53, v53
	v_pk_mul_f32 v[26:27], v[18:19], v[30:31]
	v_min_f32_e32 v18, 0x40e00000, v24
	v_min_f32_e32 v19, 0x40e00000, v25
	v_pk_mul_f32 v[30:31], v[18:19], s[28:29] op_sel_hi:[1,0]
	v_med3_f32 v24, v32, s19, v227
	v_exp_f32_e32 v30, v30
	v_exp_f32_e32 v31, v31
	v_med3_f32 v25, v33, s19, v227
	v_pk_add_f32 v[24:25], v[24:25], 1.0 op_sel_hi:[1,0]
	v_pk_fma_f32 v[6:7], v[46:47], s[24:25], v[6:7] op_sel_hi:[1,0,1]
	v_pk_add_f32 v[30:31], v[30:31], 1.0 op_sel_hi:[1,0]
	v_pk_mul_f32 v[18:19], v[18:19], v[24:25]
	v_rcp_f32_e32 v30, v30
	v_rcp_f32_e32 v31, v31
	v_pk_fma_f32 v[10:11], v[38:39], s[24:25], v[10:11] op_sel_hi:[1,0,1]
	v_med3_f32 v6, v6, s19, v227
	v_med3_f32 v7, v7, s19, v227
	v_pk_mul_f32 v[20:21], v[20:21], v[52:53]
	v_pk_mul_f32 v[24:25], v[18:19], v[30:31]
	v_mov_b32_e32 v18, v1
	v_pk_fma_f32 v[12:13], v[40:41], s[24:25], v[12:13] op_sel_hi:[1,0,1]
	v_min_f32_e32 v10, 0x40e00000, v10
	v_min_f32_e32 v11, 0x40e00000, v11
	v_pk_add_f32 v[6:7], v[6:7], 1.0 op_sel_hi:[1,0]
	v_cvt_pk_fp8_f32 v18, v20, v21
	v_pk_mul_f32 v[20:21], v[10:11], s[28:29] op_sel_hi:[1,0]
	v_pk_mul_f32 v[6:7], v[10:11], v[6:7]
	v_min_f32_e32 v10, 0x40e00000, v12
	v_min_f32_e32 v11, 0x40e00000, v13
	v_pk_mul_f32 v[12:13], v[10:11], s[28:29] op_sel_hi:[1,0]
	v_pk_fma_f32 v[8:9], v[48:49], s[24:25], v[8:9] op_sel_hi:[1,0,1]
	v_exp_f32_e32 v12, v12
	v_exp_f32_e32 v13, v13
	v_med3_f32 v8, v8, s19, v227
	v_med3_f32 v9, v9, s19, v227
	v_pk_fma_f32 v[2:3], v[34:35], s[24:25], v[2:3] op_sel_hi:[1,0,1]
	v_pk_add_f32 v[12:13], v[12:13], 1.0 op_sel_hi:[1,0]
	v_pk_add_f32 v[8:9], v[8:9], 1.0 op_sel_hi:[1,0]
	v_rcp_f32_e32 v12, v12
	v_rcp_f32_e32 v13, v13
	v_pk_mul_f32 v[8:9], v[10:11], v[8:9]
	v_min_f32_e32 v2, 0x40e00000, v2
	v_min_f32_e32 v3, 0x40e00000, v3
	v_pk_mul_f32 v[8:9], v[8:9], v[12:13]
	v_pk_mul_f32 v[12:13], v[2:3], s[28:29] op_sel_hi:[1,0]
	v_pk_fma_f32 v[14:15], v[42:43], s[24:25], v[14:15] op_sel_hi:[1,0,1]
	v_exp_f32_e32 v12, v12
	v_exp_f32_e32 v13, v13
	v_exp_f32_e32 v20, v20
	v_exp_f32_e32 v21, v21
	v_med3_f32 v10, v14, s19, v227
	v_pk_add_f32 v[12:13], v[12:13], 1.0 op_sel_hi:[1,0]
	v_med3_f32 v11, v15, s19, v227
	v_rcp_f32_e32 v12, v12
	v_rcp_f32_e32 v13, v13
	v_pk_fma_f32 v[4:5], v[36:37], s[24:25], v[4:5] op_sel_hi:[1,0,1]
	v_pk_add_f32 v[10:11], v[10:11], 1.0 op_sel_hi:[1,0]
	v_min_f32_e32 v4, 0x40e00000, v4
	v_pk_mul_f32 v[2:3], v[2:3], v[10:11]
	v_min_f32_e32 v5, 0x40e00000, v5
	v_pk_mul_f32 v[2:3], v[2:3], v[12:13]
	v_pk_mul_f32 v[12:13], v[4:5], s[28:29] op_sel_hi:[1,0]
	v_pk_add_f32 v[20:21], v[20:21], 1.0 op_sel_hi:[1,0]
	v_exp_f32_e32 v12, v12
	v_exp_f32_e32 v13, v13
	v_rcp_f32_e32 v20, v20
	v_rcp_f32_e32 v21, v21
	v_mov_b32_e32 v19, v1
	v_pk_add_f32 v[12:13], v[12:13], 1.0 op_sel_hi:[1,0]
	v_pk_fma_f32 v[16:17], v[44:45], s[24:25], v[16:17] op_sel_hi:[1,0,1]
	v_pk_mul_f32 v[6:7], v[6:7], v[20:21]
	v_rcp_f32_e32 v12, v12
	v_rcp_f32_e32 v13, v13
	v_mov_b32_e32 v20, v1
	v_mov_b32_e32 v21, v1
	v_cvt_pk_fp8_f32 v19, v26, v27
	v_med3_f32 v10, v16, s19, v227
	v_med3_f32 v11, v17, s19, v227
	v_cvt_pk_fp8_f32 v20, v6, v7
	v_cvt_pk_fp8_f32 v21, v2, v3
	v_pk_add_f32 v[10:11], v[10:11], 1.0 op_sel_hi:[1,0]
	v_add_u32_e32 v2, 0xa0, v22
	v_pk_mul_f32 v[4:5], v[4:5], v[10:11]
	v_ashrrev_i32_e32 v3, 31, v2
	v_pk_mul_f32 v[4:5], v[4:5], v[12:13]
	v_cvt_pk_fp8_f32 v18, v28, v29 op_sel:[0,0,1]
	v_cvt_pk_fp8_f32 v19, v24, v25 op_sel:[0,0,1]
	v_cvt_pk_fp8_f32 v20, v8, v9 op_sel:[0,0,1]
	v_cvt_pk_fp8_f32 v21, v4, v5 op_sel:[0,0,1]
	v_lshlrev_b64 v[2:3], 10, v[2:3]
	v_lshl_add_u64 v[2:3], s[50:51], 0, v[2:3]
	v_lshl_add_u64 v[2:3], v[2:3], 0, s[66:67]
	v_lshl_add_u64 v[2:3], v[2:3], 0, s[52:53]
	v_permlane16_swap_b32_e32 v18, v20
	v_permlane16_swap_b32_e32 v19, v21
	v_lshl_add_u64 v[2:3], v[2:3], 0, v[166:167]
	global_store_dwordx4 v[2:3], v[18:21], off
	s_cbranch_vccnz .LBB0_237
	s_andn2_b64 vcc, exec, s[42:43]
	s_cbranch_vccnz .LBB0_236
	s_barrier
	s_branch .LBB0_236
